# P11 sweeps: record address kept in a VGPR (no v_mov per batch), first-row gather address in 2 ops
# baseline (speedup 1.0000x reference)
; #define LAS __attribute__((address_space(3)))
; #define LDS_WAIT() asm volatile("s_waitcnt lgkmcnt(0)" ::: "memory")
; #define PE_VMW "vmcnt(" PE_STR(PE_VMY) ")"
; #define PE_ISSUE_U(S, rec_) PE_ISSUE4(S, rec_, UB8)
; #define PE_WAIT4U(S, cntstr) asm volatile("s_waitcnt " cntstr : "+v"(ru4[S][0]), "+v"(ru4[S][1]), "+v"(ru4[S][2]), "+v"(ru4[S][3]) :: "memory")
;     ...
;     if (lane < 2 * PE_RD_N) *(LAS v4u*)(ents + 4 * (nb + lane)) = (v4u){0u, 0u, 0u, 0u};
;     LDS_WAIT(); asm volatile("" ::: "memory");
;     ...
;     {
;         unsigned er[PE_RD];
; #pragma unroll
;         for (int q = 0; q < PE_RD; ++q) { const v4u rec = *(const LAS v4u*)(ents + 4 * q); er[q] = __builtin_amdgcn_readfirstlane(rec.x); PE_ISSUE_U(q, rec); }
;         int jcur = (int)((er[0] >> 14) & 3u);
;         v4u hcur = *(const LAS v4u*)(hql + (jcur * 64 + lane) * 4);
;         v4u nrec = *(const LAS v4u*)(ents + 4 * PE_RD);
; #pragma unroll 1
;         for (int bi = 0; bi < nb; bi += PE_RD) {
; #pragma unroll
;             for (int q = 0; q < PE_RD; ++q) {
;                 PE_WAIT4U(q, PE_VMW);
;                 PE_UBATCH(q, er[q]);
;                 er[q] = __builtin_amdgcn_readfirstlane(nrec.x);
;                 PE_ISSUE_U(q, nrec);
;                 nrec = *(const LAS v4u*)(ents + 4 * (bi + q + PE_RD + 1));
.LBB0_2832:
	s_or_b64 exec, exec, s[0:1]
	v_cmp_gt_i32_e32 vcc, 6, v50
	s_and_saveexec_b64 s[0:1], vcc
	v_add_u32_e32 v0, s6, v50
	v_lshl_add_u32 v0, v0, 4, s90
	ds_write_b128 v0, v[122:125] offset:6720
	s_or_b64 exec, exec, s[0:1]
	s_waitcnt lgkmcnt(0)
	v_mov_b32_e32 v5, s90
	ds_read_b128 v[0:3], v5 offset:6720
	v_lshlrev_b32_e32 v118, 3, v50
	v_and_b32_e32 v43, 31, v50
	v_cmp_lt_u32_e64 s[100:101], 31, v50
	v_lshlrev_b32_e32 v43, 4, v43
	v_lshl_add_u32 v52, v43, 1, s90
	s_cmp_gt_i32 s6, 0
	s_cselect_b64 s[2:3], -1, 0
	s_cmp_lt_i32 s6, 1
	s_waitcnt lgkmcnt(0)
	v_readfirstlane_b32 s10, v0
	v_and_b32_e32 v48, 0x3fff, v0
	v_cndmask_b32_e64 v48, v48, v1, s[100:101]
	v_lshl_add_u32 v48, v48, 9, v43
	global_load_dwordx4 v[8:11], v48, s[70:71]
	v_cndmask_b32_e64 v48, v2, v3, s[100:101]
	v_lshl_add_u32 v48, v48, 9, v43
	global_load_dwordx4 v[12:15], v48, s[70:71]
	ds_read_b128 v[0:3], v5 offset:6736
	s_waitcnt lgkmcnt(0)
	v_readfirstlane_b32 s11, v0
	v_and_b32_e32 v48, 0x3fff, v0
	v_cndmask_b32_e64 v48, v48, v1, s[100:101]
	v_lshl_add_u32 v48, v48, 9, v43
	global_load_dwordx4 v[16:19], v48, s[70:71]
	v_cndmask_b32_e64 v48, v2, v3, s[100:101]
	v_lshl_add_u32 v48, v48, 9, v43
	global_load_dwordx4 v[20:23], v48, s[70:71]
	ds_read_b128 v[0:3], v5 offset:6752
	s_waitcnt lgkmcnt(0)
	v_readfirstlane_b32 s12, v0
	v_and_b32_e32 v48, 0x3fff, v0
	v_cndmask_b32_e64 v48, v48, v1, s[100:101]
	v_lshl_add_u32 v48, v48, 9, v43
	global_load_dwordx4 v[24:27], v48, s[70:71]
	v_cndmask_b32_e64 v48, v2, v3, s[100:101]
	v_lshl_add_u32 v48, v48, 9, v43
	global_load_dwordx4 v[28:31], v48, s[70:71]
	s_cbranch_scc1 .LBB0_2861
	s_bfe_u32 s9, s10, 0x2000e
	v_lshl_add_u32 v48, s9, 10, v52
	ds_read_b128 v[0:3], v48 offset:11072
	ds_read_b128 v[44:47], v48 offset:11088
	v_and_b32_e32 v4, 15, v50
	v_bfe_u32 v33, v50, 4, 1
	v_cmp_eq_u32_e32 vcc, 0, v4
	v_lshrrev_b32_e32 v4, 5, v50
	s_mov_b32 s7, 0
	v_lshl_add_u32 v33, v33, 1, v4
	v_readlane_b32 s8, v255, 2
	s_nop 1
	v_mov_b32_e32 v136, s8
.LBB0_2838:
	ds_read_b128 v[4:7], v136
	s_waitcnt vmcnt(4)
	s_bfe_u32 s0, s10, 0x30010
	s_cmp_lg_u32 s0, 0
	s_cbranch_scc0 .Lu16_skip0
	s_bfe_u32 s1, s10, 0x2000e
	s_cmp_eq_u32 s1, s9
	s_cbranch_scc1 .Lu16_same0
	v_lshl_add_u32 v48, s1, 10, v52
	ds_read_b128 v[0:3], v48 offset:11072
	ds_read_b128 v[44:47], v48 offset:11088
	s_mov_b32 s9, s1

; #define LAS __attribute__((address_space(3)))
; #define PE_VMW "vmcnt(" PE_STR(PE_VMY) ")"
; #define PE_ISSUE_U(S, rec_) PE_ISSUE4(S, rec_, UB8)
; #define PE_WAIT4U(S, cntstr) asm volatile("s_waitcnt " cntstr : "+v"(ru4[S][0]), "+v"(ru4[S][1]), "+v"(ru4[S][2]), "+v"(ru4[S][3]) :: "memory")
;     ...
;             for (int q = 0; q < PE_RD; ++q) {
;                 PE_WAIT4U(q, PE_VMW);
;                 PE_UBATCH(q, er[q]);
;                 er[q] = __builtin_amdgcn_readfirstlane(nrec.x);
;                 PE_ISSUE_U(q, nrec);
;                 nrec = *(const LAS v4u*)(ents + 4 * (bi + q + PE_RD + 1));
.Lu16_skip0:
	s_waitcnt lgkmcnt(0)
	v_readfirstlane_b32 s10, v4
	v_and_b32_e32 v48, 0x3fff, v4
	v_cndmask_b32_e64 v48, v48, v5, s[100:101]
	v_lshl_add_u32 v48, v48, 9, v43
	global_load_dwordx4 v[8:11], v48, s[70:71]
	v_cndmask_b32_e64 v48, v6, v7, s[100:101]
	v_lshl_add_u32 v48, v48, 9, v43
	global_load_dwordx4 v[12:15], v48, s[70:71]
	ds_read_b128 v[4:7], v136 offset:16
	s_waitcnt vmcnt(4)
	s_bfe_u32 s0, s11, 0x30010
	s_cmp_lg_u32 s0, 0
	s_cbranch_scc0 .Lu16_skip1
	s_bfe_u32 s1, s11, 0x2000e
	s_cmp_eq_u32 s1, s9
	s_cbranch_scc1 .Lu16_same1
	v_lshl_add_u32 v48, s1, 10, v52
	ds_read_b128 v[0:3], v48 offset:11072
	ds_read_b128 v[44:47], v48 offset:11088
	s_mov_b32 s9, s1

; #define LAS __attribute__((address_space(3)))
; #define PE_VMW "vmcnt(" PE_STR(PE_VMY) ")"
; #define PE_ISSUE_U(S, rec_) PE_ISSUE4(S, rec_, UB8)
; #define PE_WAIT4U(S, cntstr) asm volatile("s_waitcnt " cntstr : "+v"(ru4[S][0]), "+v"(ru4[S][1]), "+v"(ru4[S][2]), "+v"(ru4[S][3]) :: "memory")
;     ...
;             for (int q = 0; q < PE_RD; ++q) {
;                 PE_WAIT4U(q, PE_VMW);
;                 PE_UBATCH(q, er[q]);
;                 er[q] = __builtin_amdgcn_readfirstlane(nrec.x);
;                 PE_ISSUE_U(q, nrec);
;                 nrec = *(const LAS v4u*)(ents + 4 * (bi + q + PE_RD + 1));
.Lu16_skip1:
	s_waitcnt lgkmcnt(0)
	v_readfirstlane_b32 s11, v4
	v_and_b32_e32 v48, 0x3fff, v4
	v_cndmask_b32_e64 v48, v48, v5, s[100:101]
	v_lshl_add_u32 v48, v48, 9, v43
	global_load_dwordx4 v[16:19], v48, s[70:71]
	v_cndmask_b32_e64 v48, v6, v7, s[100:101]
	v_lshl_add_u32 v48, v48, 9, v43
	global_load_dwordx4 v[20:23], v48, s[70:71]
	ds_read_b128 v[4:7], v136 offset:32
	s_waitcnt vmcnt(4)
	s_bfe_u32 s0, s12, 0x30010
	s_cmp_lg_u32 s0, 0
	s_cbranch_scc0 .Lu16_skip2
	s_bfe_u32 s1, s12, 0x2000e
	s_cmp_eq_u32 s1, s9
	s_cbranch_scc1 .Lu16_same2
	v_lshl_add_u32 v48, s1, 10, v52
	ds_read_b128 v[0:3], v48 offset:11072
	ds_read_b128 v[44:47], v48 offset:11088
	s_mov_b32 s9, s1

; #define LAS __attribute__((address_space(3)))
; #define LDS_WAIT() asm volatile("s_waitcnt lgkmcnt(0)" ::: "memory")
; #define PE_VMW "vmcnt(" PE_STR(PE_VMY) ")"
; #define PE_ISSUE_U(S, rec_) PE_ISSUE4(S, rec_, UB8)
; #define PE_WAIT4U(S, cntstr) asm volatile("s_waitcnt " cntstr : "+v"(ru4[S][0]), "+v"(ru4[S][1]), "+v"(ru4[S][2]), "+v"(ru4[S][3]) :: "memory")
;     ...
;             for (int q = 0; q < PE_RD; ++q) {
;                 PE_WAIT4U(q, PE_VMW);
;                 PE_UBATCH(q, er[q]);
;                 er[q] = __builtin_amdgcn_readfirstlane(nrec.x);
;                 PE_ISSUE_U(q, nrec);
;                 nrec = *(const LAS v4u*)(ents + 4 * (bi + q + PE_RD + 1));
;             }
;         }
; #pragma unroll
;         for (int q = 0; q < PE_RD; ++q) PE_WAIT4U(q, "vmcnt(0)");
;     }
;     LDS_WAIT(); asm volatile("" ::: "memory");
;     float wsj[PE_NT];
; #pragma unroll
;     for (int j = 0; j < PE_NT; ++j) {
;         LAS unsigned* lt = lw + j * PE_TOK_W + 128;
;         const float a0 = __builtin_bit_cast(float, lt[2 * lane]), a1 = __builtin_bit_cast(float, lt[2 * lane + 1]);
;         const float wm = fmaxf(wave_max(fmaxf(fabsf(a0), fabsf(a1))), 1e-30f), wq = 127.0f * __builtin_amdgcn_rcpf(wm);
;         wsj[j] = wm * (1.0f / 127.0f);
;         const unsigned pr = (__builtin_bit_cast(unsigned, __builtin_fmaf(a0, wq, 12582912.0f)) & 0xffu) | ((__builtin_bit_cast(unsigned, __builtin_fmaf(a1, wq, 12582912.0f)) & 0xffu) << 8);
;         const unsigned nbp = (unsigned)__builtin_amdgcn_update_dpp(0, (int)pr, 0xB1, 0xF, 0xF, true);
;         asm volatile("" ::: "memory");
;         if ((lane & 1) == 0) lt[2 * lane] = pr | (nbp << 16);
;     }
.Lu16_skip2:
	s_waitcnt lgkmcnt(0)
	v_readfirstlane_b32 s12, v4
	v_and_b32_e32 v48, 0x3fff, v4
	v_cndmask_b32_e64 v48, v48, v5, s[100:101]
	v_lshl_add_u32 v48, v48, 9, v43
	global_load_dwordx4 v[24:27], v48, s[70:71]
	v_cndmask_b32_e64 v48, v6, v7, s[100:101]
	v_lshl_add_u32 v48, v48, 9, v43
	global_load_dwordx4 v[28:31], v48, s[70:71]
	s_add_i32 s7, s7, 3
	s_add_i32 s8, s8, 48
	v_add_u32_e32 v136, 48, v136
	s_cmp_ge_i32 s7, s6
	s_cbranch_scc0 .LBB0_2838
.LBB0_2861:
	s_waitcnt vmcnt(0)
	s_waitcnt vmcnt(0)
	s_waitcnt vmcnt(0)
	s_waitcnt lgkmcnt(0)
	v_add_u32_e32 v1, s90, v118
	ds_read_b64 v[126:127], v1
	ds_read_b64 v[128:129], v1 offset:1024
	ds_read_b64 v[2:3], v1 offset:512
	s_mov_b32 s0, 0xc0c0500
	v_and_b32_e32 v5, 1, v50
	v_cmp_eq_u32_e32 vcc, 0, v5
	s_waitcnt lgkmcnt(0)
	v_cvt_f32_i32_e32 v126, v126
	v_cvt_f32_i32_e32 v127, v127
	v_mul_f32_e32 v126, v128, v126
	v_mul_f32_e32 v127, v129, v127
	v_mul_f32_e32 v94, v126, v126
	v_mul_f32_e32 v95, v127, v127
	v_fmamk_f32 v94, v94, 0xbdd2d3e8, v113
	v_fmamk_f32 v95, v95, 0xbdd2d3e8, v113
	v_mul_f32_e32 v94, v126, v94
	v_mul_f32_e32 v95, v127, v95
	v_exp_f32_e32 v94, v94
	v_exp_f32_e32 v95, v95
	s_nop 0
	v_add_f32_e32 v94, 1.0, v94
	v_add_f32_e32 v95, 1.0, v95
	v_rcp_f32_e32 v94, v94
	v_rcp_f32_e32 v95, v95
	s_nop 0
	v_mul_f32_e32 v126, v126, v94
	v_mul_f32_e32 v127, v127, v95
	v_mul_f32_e32 v2, v2, v126
	v_mul_f32_e32 v3, v3, v127
	v_max_f32_e64 v0, |v3|, |v3|
	v_max_f32_e64 v4, |v2|, |v2|
	v_max_f32_e32 v0, v4, v0
	s_nop 1
	v_mov_b32_dpp v4, v0 quad_perm:[1,0,3,2] row_mask:0xf bank_mask:0xf bound_ctrl:1
	v_max_f32_e32 v4, v4, v4
	v_max_f32_e32 v0, v0, v4
	s_nop 1
	v_mov_b32_dpp v4, v0 quad_perm:[2,3,0,1] row_mask:0xf bank_mask:0xf bound_ctrl:1
	v_max_f32_e32 v4, v4, v4
	v_max_f32_e32 v0, v0, v4
	s_nop 1
	v_mov_b32_dpp v4, v0 row_half_mirror row_mask:0xf bank_mask:0xf bound_ctrl:1
	v_max_f32_e32 v4, v4, v4
	v_max_f32_e32 v0, v0, v4
	s_nop 1
	v_mov_b32_dpp v4, v0 row_mirror row_mask:0xf bank_mask:0xf bound_ctrl:1
	v_max_f32_e32 v4, v4, v4
	v_max_f32_e32 v0, v0, v4
	v_mov_b32_e32 v4, v0
	s_nop 1
	v_permlane16_swap_b32_e32 v0, v4
	v_max_f32 v0, v0, v4
	s_nop 1
	s_nop 0
	v_mov_b32_e32 v4, v0
	s_nop 1
	v_permlane32_swap_b32_e32 v0, v4
	v_max_f32 v0, v0, v4
	s_nop 0
	v_max_f32_e32 v0, v0, v0
	v_max_f32_e32 v0, 0xda24260, v0
	v_rcp_f32_e32 v4, v0
	s_nop 0
	v_mul_f32_e32 v4, 0x42fe0000, v4
	v_fmaak_f32 v3, v3, v4, 0x4b400000
	v_fmaak_f32 v2, v2, v4, 0x4b400000
	v_lshlrev_b32_e32 v3, 8, v3
	v_perm_b32 v2, v3, v2, s0
	s_nop 1
	v_mov_b32_dpp v3, v2 quad_perm:[1,0,3,2] row_mask:0xf bank_mask:0xf bound_ctrl:1
	s_and_saveexec_b64 s[0:1], vcc
	v_lshl_or_b32 v2, v3, 16, v2
	ds_write_b32 v1, v2 offset:512
	s_or_b64 exec, exec, s[0:1]
	ds_read_b64 v[126:127], v1 offset:1680
	ds_read_b64 v[128:129], v1 offset:2704
	ds_read_b64 v[4:5], v1 offset:2192
	s_mov_b32 s0, 0xc0c0500
	s_waitcnt lgkmcnt(0)
	v_cvt_f32_i32_e32 v126, v126
	v_cvt_f32_i32_e32 v127, v127
	v_mul_f32_e32 v126, v128, v126
	v_mul_f32_e32 v127, v129, v127
	v_mul_f32_e32 v94, v126, v126
	v_mul_f32_e32 v95, v127, v127
	v_fmamk_f32 v94, v94, 0xbdd2d3e8, v113
	v_fmamk_f32 v95, v95, 0xbdd2d3e8, v113
	v_mul_f32_e32 v94, v126, v94
	v_mul_f32_e32 v95, v127, v95
	v_exp_f32_e32 v94, v94
	v_exp_f32_e32 v95, v95
	s_nop 0
	v_add_f32_e32 v94, 1.0, v94
	v_add_f32_e32 v95, 1.0, v95
	v_rcp_f32_e32 v94, v94
	v_rcp_f32_e32 v95, v95
	s_nop 0
	v_mul_f32_e32 v126, v126, v94
	v_mul_f32_e32 v127, v127, v95
	v_mul_f32_e32 v4, v4, v126
	v_mul_f32_e32 v5, v5, v127
	v_max_f32_e64 v2, |v5|, |v5|
	v_max_f32_e64 v3, |v4|, |v4|
	v_max_f32_e32 v2, v3, v2
	s_nop 1
	v_mov_b32_dpp v3, v2 quad_perm:[1,0,3,2] row_mask:0xf bank_mask:0xf bound_ctrl:1
	v_max_f32_e32 v3, v3, v3
	v_max_f32_e32 v2, v2, v3
	s_nop 1
	v_mov_b32_dpp v3, v2 quad_perm:[2,3,0,1] row_mask:0xf bank_mask:0xf bound_ctrl:1
	v_max_f32_e32 v3, v3, v3
	v_max_f32_e32 v2, v2, v3
	s_nop 1
	v_mov_b32_dpp v3, v2 row_half_mirror row_mask:0xf bank_mask:0xf bound_ctrl:1
	v_max_f32_e32 v3, v3, v3
	v_max_f32_e32 v2, v2, v3
	s_nop 1
	v_mov_b32_dpp v3, v2 row_mirror row_mask:0xf bank_mask:0xf bound_ctrl:1
	v_max_f32_e32 v3, v3, v3
	v_max_f32_e32 v2, v2, v3
	v_mov_b32_e32 v3, v2
	s_nop 1
	v_permlane16_swap_b32_e32 v2, v3
	v_max_f32 v2, v2, v3
	s_nop 1
	s_nop 0
	v_mov_b32_e32 v3, v2
	s_nop 1
	v_permlane32_swap_b32_e32 v2, v3
	v_max_f32 v2, v2, v3
	s_nop 0
	v_max_f32_e32 v2, v2, v2
	v_max_f32_e32 v2, 0xda24260, v2
	v_rcp_f32_e32 v3, v2
	s_nop 0
	v_mul_f32_e32 v3, 0x42fe0000, v3
	v_fmaak_f32 v4, v4, v3, 0x4b400000
	v_fmaak_f32 v3, v5, v3, 0x4b400000
	v_lshlrev_b32_e32 v3, 8, v3
	v_perm_b32 v3, v3, v4, s0
	s_nop 1
	v_mov_b32_dpp v4, v3 quad_perm:[1,0,3,2] row_mask:0xf bank_mask:0xf bound_ctrl:1
	s_and_saveexec_b64 s[0:1], vcc
	v_lshl_or_b32 v3, v4, 16, v3
	ds_write_b32 v1, v3 offset:2192
	s_or_b64 exec, exec, s[0:1]
	ds_read_b64 v[126:127], v1 offset:3360
	ds_read_b64 v[128:129], v1 offset:4384
	ds_read_b64 v[4:5], v1 offset:3872
	s_mov_b32 s0, 0xc0c0500
	s_waitcnt lgkmcnt(0)
; #define LAS __attribute__((address_space(3)))
; #define LDS_WAIT() asm volatile("s_waitcnt lgkmcnt(0)" ::: "memory")
;     ...
;     for (int j = 0; j < PE_NT; ++j) {
;         LAS unsigned* lt = lw + j * PE_TOK_W + 128;
;         const float a0 = __builtin_bit_cast(float, lt[2 * lane]), a1 = __builtin_bit_cast(float, lt[2 * lane + 1]);
;         const float wm = fmaxf(wave_max(fmaxf(fabsf(a0), fabsf(a1))), 1e-30f), wq = 127.0f * __builtin_amdgcn_rcpf(wm);
;         wsj[j] = wm * (1.0f / 127.0f);
;         const unsigned pr = (__builtin_bit_cast(unsigned, __builtin_fmaf(a0, wq, 12582912.0f)) & 0xffu) | ((__builtin_bit_cast(unsigned, __builtin_fmaf(a1, wq, 12582912.0f)) & 0xffu) << 8);
;         const unsigned nbp = (unsigned)__builtin_amdgcn_update_dpp(0, (int)pr, 0xB1, 0xF, 0xF, true);
;         asm volatile("" ::: "memory");
;         if ((lane & 1) == 0) lt[2 * lane] = pr | (nbp << 16);
;     }
;     LDS_WAIT(); asm volatile("" ::: "memory");
;     {
;         unsigned er[PE_RD];
; #pragma unroll
;         for (int q = 0; q < PE_RD; ++q) { const v4u rec = *(const LAS v4u*)(ents + 4 * q); er[q] = __builtin_amdgcn_readfirstlane(rec.x); PE_ISSUE4(q, rec, VB8); }
;         int curi[16];
; #pragma unroll
;         for (int i = 0; i < 16; ++i) curi[i] = 0;
;         int jcur = (int)((er[0] >> 14) & 3u);
;         v4u nrec = *(const LAS v4u*)(ents + 4 * PE_RD);
	v_cvt_f32_i32_e32 v126, v126
	v_cvt_f32_i32_e32 v127, v127
	v_mul_f32_e32 v126, v128, v126
	v_mul_f32_e32 v127, v129, v127
	v_mul_f32_e32 v94, v126, v126
	v_mul_f32_e32 v95, v127, v127
	v_fmamk_f32 v94, v94, 0xbdd2d3e8, v113
	v_fmamk_f32 v95, v95, 0xbdd2d3e8, v113
	v_mul_f32_e32 v94, v126, v94
	v_mul_f32_e32 v95, v127, v95
	v_exp_f32_e32 v94, v94
	v_exp_f32_e32 v95, v95
	s_nop 0
	v_add_f32_e32 v94, 1.0, v94
	v_add_f32_e32 v95, 1.0, v95
	v_rcp_f32_e32 v94, v94
	v_rcp_f32_e32 v95, v95
	s_nop 0
	v_mul_f32_e32 v126, v126, v94
	v_mul_f32_e32 v127, v127, v95
	v_mul_f32_e32 v4, v4, v126
	v_mul_f32_e32 v5, v5, v127
	v_max_f32_e64 v3, |v5|, |v5|
	v_max_f32_e64 v6, |v4|, |v4|
	v_max_f32_e32 v3, v6, v3
	s_nop 1
	v_mov_b32_dpp v6, v3 quad_perm:[1,0,3,2] row_mask:0xf bank_mask:0xf bound_ctrl:1
	v_max_f32_e32 v6, v6, v6
	v_max_f32_e32 v3, v3, v6
	s_nop 1
	v_mov_b32_dpp v6, v3 quad_perm:[2,3,0,1] row_mask:0xf bank_mask:0xf bound_ctrl:1
	v_max_f32_e32 v6, v6, v6
	v_max_f32_e32 v3, v3, v6
	s_nop 1
	v_mov_b32_dpp v6, v3 row_half_mirror row_mask:0xf bank_mask:0xf bound_ctrl:1
	v_max_f32_e32 v6, v6, v6
	v_max_f32_e32 v3, v3, v6
	s_nop 1
	v_mov_b32_dpp v6, v3 row_mirror row_mask:0xf bank_mask:0xf bound_ctrl:1
	v_max_f32_e32 v6, v6, v6
	v_max_f32_e32 v3, v3, v6
	v_mov_b32_e32 v6, v3
	s_nop 1
	v_permlane16_swap_b32_e32 v3, v6
	v_max_f32 v3, v3, v6
	s_nop 1
	s_nop 0
	v_mov_b32_e32 v6, v3
	s_nop 1
	v_permlane32_swap_b32_e32 v3, v6
	v_max_f32 v3, v3, v6
	s_nop 0
	v_max_f32_e32 v3, v3, v3
	v_max_f32_e32 v3, 0xda24260, v3
	v_rcp_f32_e32 v6, v3
	s_nop 0
	v_mul_f32_e32 v6, 0x42fe0000, v6
	v_fmaak_f32 v5, v5, v6, 0x4b400000
	v_fmaak_f32 v4, v4, v6, 0x4b400000
	v_lshlrev_b32_e32 v5, 8, v5
	v_perm_b32 v4, v5, v4, s0
	s_nop 1
	v_mov_b32_dpp v5, v4 quad_perm:[1,0,3,2] row_mask:0xf bank_mask:0xf bound_ctrl:1
	s_and_saveexec_b64 s[0:1], vcc
	v_lshl_or_b32 v4, v5, 16, v4
	ds_write_b32 v1, v4 offset:3872
	s_or_b64 exec, exec, s[0:1]
	ds_read_b64 v[126:127], v1 offset:5040
	ds_read_b64 v[128:129], v1 offset:6064
	ds_read_b64 v[6:7], v1 offset:5552
	s_mov_b32 s0, 0xc0c0500
	s_waitcnt lgkmcnt(0)
	v_cvt_f32_i32_e32 v126, v126
	v_cvt_f32_i32_e32 v127, v127
	v_mul_f32_e32 v126, v128, v126
	v_mul_f32_e32 v127, v129, v127
	v_mul_f32_e32 v94, v126, v126
	v_mul_f32_e32 v95, v127, v127
	v_fmamk_f32 v94, v94, 0xbdd2d3e8, v113
	v_fmamk_f32 v95, v95, 0xbdd2d3e8, v113
	v_mul_f32_e32 v94, v126, v94
	v_mul_f32_e32 v95, v127, v95
	v_exp_f32_e32 v94, v94
	v_exp_f32_e32 v95, v95
	s_nop 0
	v_add_f32_e32 v94, 1.0, v94
	v_add_f32_e32 v95, 1.0, v95
	v_rcp_f32_e32 v94, v94
	v_rcp_f32_e32 v95, v95
	s_nop 0
	v_mul_f32_e32 v126, v126, v94
	v_mul_f32_e32 v127, v127, v95
	v_mul_f32_e32 v6, v6, v126
	v_mul_f32_e32 v7, v7, v127
	v_max_f32_e64 v4, |v7|, |v7|
	v_max_f32_e64 v5, |v6|, |v6|
	v_max_f32_e32 v4, v5, v4
	s_nop 1
	v_mov_b32_dpp v5, v4 quad_perm:[1,0,3,2] row_mask:0xf bank_mask:0xf bound_ctrl:1
	v_max_f32_e32 v5, v5, v5
	v_max_f32_e32 v4, v4, v5
	s_nop 1
	v_mov_b32_dpp v5, v4 quad_perm:[2,3,0,1] row_mask:0xf bank_mask:0xf bound_ctrl:1
	v_max_f32_e32 v5, v5, v5
	v_max_f32_e32 v4, v4, v5
	s_nop 1
	v_mov_b32_dpp v5, v4 row_half_mirror row_mask:0xf bank_mask:0xf bound_ctrl:1
	v_max_f32_e32 v5, v5, v5
	v_max_f32_e32 v4, v4, v5
	s_nop 1
	v_mov_b32_dpp v5, v4 row_mirror row_mask:0xf bank_mask:0xf bound_ctrl:1
	v_max_f32_e32 v5, v5, v5
	v_max_f32_e32 v4, v4, v5
	v_mov_b32_e32 v5, v4
	s_nop 1
	v_permlane16_swap_b32_e32 v4, v5
	v_max_f32 v4, v4, v5
	s_nop 1
	s_nop 0
	v_mov_b32_e32 v5, v4
	s_nop 1
	v_permlane32_swap_b32_e32 v4, v5
	v_max_f32 v4, v4, v5
	s_nop 0
	v_max_f32_e32 v4, v4, v4
	v_max_f32_e32 v4, 0xda24260, v4
	v_rcp_f32_e32 v5, v4
	s_nop 0
	v_mul_f32_e32 v5, 0x42fe0000, v5
	v_fmaak_f32 v6, v6, v5, 0x4b400000
	v_fmaak_f32 v5, v7, v5, 0x4b400000
	v_lshlrev_b32_e32 v5, 8, v5
	v_perm_b32 v5, v5, v6, s0
	s_nop 1
	v_mov_b32_dpp v6, v5 quad_perm:[1,0,3,2] row_mask:0xf bank_mask:0xf bound_ctrl:1
	s_and_saveexec_b64 s[0:1], vcc
	v_lshl_or_b32 v5, v6, 16, v5
	ds_write_b32 v1, v5 offset:5552
	s_or_b64 exec, exec, s[0:1]
	s_waitcnt lgkmcnt(0)
	v_mov_b32_e32 v1, s90
	ds_read_b128 v[6:9], v1 offset:6720
	v_mul_f32_e32 v119, 0x3c010204, v3
	v_mul_f32_e32 v117, 0x3c010204, v4
	v_mul_f32_e32 v121, 0x3c010204, v0
	v_mul_f32_e32 v120, 0x3c010204, v2
	s_waitcnt lgkmcnt(0)
	v_lshlrev_b32_e32 v5, 9, v6
	v_and_b32_e32 v5, 0x7ffe00, v5
	v_add_u32_e32 v5, v5, v118
	global_load_dwordx2 v[70:71], v5, s[82:83]
	v_lshl_add_u32 v7, v7, 9, v118
	global_load_dwordx2 v[72:73], v7, s[82:83]
	v_lshl_add_u32 v8, v8, 9, v118
	global_load_dwordx2 v[74:75], v8, s[82:83]
	v_lshl_add_u32 v9, v9, 9, v118
	global_load_dwordx2 v[80:81], v9, s[82:83]
	ds_read_b128 v[8:11], v1 offset:6736
	v_readfirstlane_b32 s4, v6
	s_bfe_u32 s7, s4, 0x2000e
	s_andn2_b64 vcc, exec, s[2:3]
	s_mov_b32 s0, 0
	s_waitcnt lgkmcnt(0)
	v_lshlrev_b32_e32 v3, 9, v8
	v_and_b32_e32 v3, 0x7ffe00, v3
	v_add_u32_e32 v3, v3, v118
	global_load_dwordx2 v[76:77], v3, s[82:83]
	v_lshl_add_u32 v4, v9, 9, v118
	global_load_dwordx2 v[82:83], v4, s[82:83]
	v_lshl_add_u32 v5, v10, 9, v118
	global_load_dwordx2 v[84:85], v5, s[82:83]
	v_lshl_add_u32 v3, v11, 9, v118
	global_load_dwordx2 v[90:91], v3, s[82:83]
	ds_read_b128 v[10:13], v1 offset:6752
	v_readfirstlane_b32 s5, v8
	s_waitcnt lgkmcnt(0)
	v_lshlrev_b32_e32 v0, 9, v10
	v_and_b32_e32 v0, 0x7ffe00, v0
	v_add_u32_e32 v0, v0, v118
	global_load_dwordx2 v[78:79], v0, s[82:83]
	v_lshl_add_u32 v0, v11, 9, v118
	global_load_dwordx2 v[86:87], v0, s[82:83]
	v_lshl_add_u32 v0, v12, 9, v118
	global_load_dwordx2 v[88:89], v0, s[82:83]
	v_lshl_add_u32 v0, v13, 9, v118
	global_load_dwordx2 v[92:93], v0, s[82:83]
	v_readfirstlane_b32 s8, v10
	s_cbranch_vccnz .LBB0_2884
; #define LAS __attribute__((address_space(3)))
;     ...
;         int curi[16];
; #pragma unroll
;         for (int i = 0; i < 16; ++i) curi[i] = 0;
;         int jcur = (int)((er[0] >> 14) & 3u);
;         v4u nrec = *(const LAS v4u*)(ents + 4 * PE_RD);
	v_mov_b32_e32 v48, v49
	v_mov_b32_e32 v130, 0x1010101
	v_mov_b32_e32 v131, 0
	v_mov_b32_e32 v132, 0
	v_mov_b32_e32 v133, 0
	v_mov_b32_e32 v134, 0
	v_mov_b32_e32 v94, 0
	v_mov_b32_e32 v95, 0
	v_mov_b32_e32 v96, 0
	v_mov_b32_e32 v97, 0
	v_mov_b32_e32 v98, 0
	v_mov_b32_e32 v99, 0
	v_mov_b32_e32 v100, 0
	v_mov_b32_e32 v101, 0
	v_mov_b32_e32 v102, 0
	v_mov_b32_e32 v103, 0
	v_mov_b32_e32 v104, 0
	v_mov_b32_e32 v105, 0
	v_mov_b32_e32 v106, 0
	v_mov_b32_e32 v107, 0
	v_mov_b32_e32 v108, 0
	v_mov_b32_e32 v109, 0
	v_readlane_b32 s1, v255, 2
	v_mov_b64_e32 v[12:13], v[48:49]
	v_mov_b64_e32 v[14:15], v[48:49]
	v_mov_b64_e32 v[16:17], v[48:49]
	v_mov_b64_e32 v[18:19], v[48:49]
	v_mov_b64_e32 v[34:35], v[48:49]
	v_mov_b64_e32 v[32:33], v[48:49]
	v_mov_b64_e32 v[30:31], v[48:49]
	v_mov_b64_e32 v[28:29], v[48:49]
	v_mov_b64_e32 v[26:27], v[48:49]
	v_mov_b64_e32 v[24:25], v[48:49]
	v_mov_b64_e32 v[22:23], v[48:49]
	v_mov_b64_e32 v[20:21], v[48:49]
	v_mov_b64_e32 v[52:53], v[48:49]
	v_mov_b64_e32 v[50:51], v[48:49]
	v_mov_b64_e32 v[46:47], v[48:49]
	v_mov_b64_e32 v[44:45], v[48:49]
	v_mov_b64_e32 v[42:43], v[48:49]
	v_mov_b64_e32 v[40:41], v[48:49]
	v_mov_b64_e32 v[38:39], v[48:49]
	v_mov_b64_e32 v[36:37], v[48:49]
	v_mov_b64_e32 v[68:69], v[48:49]
	v_mov_b64_e32 v[66:67], v[48:49]
	v_mov_b64_e32 v[64:65], v[48:49]
	v_mov_b64_e32 v[62:63], v[48:49]
	v_mov_b64_e32 v[60:61], v[48:49]
	v_mov_b64_e32 v[58:59], v[48:49]
	v_mov_b64_e32 v[56:57], v[48:49]
	v_mov_b64_e32 v[54:55], v[48:49]
	v_mov_b64_e32 v[10:11], v[48:49]
	v_mov_b64_e32 v[8:9], v[48:49]
	v_mov_b64_e32 v[6:7], v[48:49]
	v_mov_b64_e32 v[4:5], v[48:49]
	v_mov_b32_e32 v135, s1
	s_branch .LBB0_2873

; #define LAS __attribute__((address_space(3)))
; #define PE_VMW "vmcnt(" PE_STR(PE_VMY) ")"
; #define PE_WAIT4U(S, cntstr) asm volatile("s_waitcnt " cntstr : "+v"(ru4[S][0]), "+v"(ru4[S][1]), "+v"(ru4[S][2]), "+v"(ru4[S][3]) :: "memory")
;     ...
;         for (int bi = 0; bi < nb; bi += PE_RD) {
; #pragma unroll
;             for (int q = 0; q < PE_RD; ++q) {
;                 PE_WAIT4U(q, PE_VMW);
;                 PE_VBATCH(q, er[q]);
;                 er[q] = __builtin_amdgcn_readfirstlane(nrec.x);
;                 PE_ISSUE4(q, nrec, VB8);
;                 nrec = *(const LAS v4u*)(ents + 4 * (bi + q + PE_RD + 1));
;             }
.LBB0_2872:
	s_waitcnt lgkmcnt(0)
	v_readfirstlane_b32 s8, v0
	v_and_b32_e32 v0, 0x3fff, v0
	v_lshl_add_u32 v0, v0, 9, v118
	global_load_dwordx2 v[78:79], v0, s[82:83]
	v_lshl_add_u32 v0, v1, 9, v118
	global_load_dwordx2 v[86:87], v0, s[82:83]
	v_lshl_add_u32 v0, v2, 9, v118
	global_load_dwordx2 v[88:89], v0, s[82:83]
	v_lshl_add_u32 v0, v3, 9, v118
	global_load_dwordx2 v[92:93], v0, s[82:83]
	s_add_i32 s0, s0, 3
	s_add_i32 s1, s1, 48
	v_add_u32_e32 v135, 48, v135
	s_cmp_ge_i32 s0, s6
	s_cbranch_scc1 .LBB0_2677
.LBB0_2873:
	ds_read_b128 v[0:3], v135
	s_waitcnt vmcnt(8)
	s_and_b32 s2, s4, 0x70000
	s_cmp_lg_u32 s2, 0
	s_cbranch_scc0 .LBB0_2877
	s_bfe_u32 s2, s4, 0x2000e
	s_cmp_eq_u32 s2, 0
	s_cbranch_scc1 .LvA_t0
	s_cmp_eq_u32 s2, 1
	s_cbranch_scc1 .LvA_t1
	s_cmp_eq_u32 s2, 2
	s_cbranch_scc1 .LvA_t2
	s_branch .LvA_t3

; #define LAS __attribute__((address_space(3)))
; #define PE_VMW "vmcnt(" PE_STR(PE_VMY) ")"
; #define PE_WAIT4U(S, cntstr) asm volatile("s_waitcnt " cntstr : "+v"(ru4[S][0]), "+v"(ru4[S][1]), "+v"(ru4[S][2]), "+v"(ru4[S][3]) :: "memory")
;     ...
;         for (int bi = 0; bi < nb; bi += PE_RD) {
; #pragma unroll
;             for (int q = 0; q < PE_RD; ++q) {
;                 PE_WAIT4U(q, PE_VMW);
;                 PE_VBATCH(q, er[q]);
;                 er[q] = __builtin_amdgcn_readfirstlane(nrec.x);
;                 PE_ISSUE4(q, nrec, VB8);
;                 nrec = *(const LAS v4u*)(ents + 4 * (bi + q + PE_RD + 1));
;             }
.LBB0_2877:
	s_waitcnt lgkmcnt(0)
	v_readfirstlane_b32 s4, v0
	v_and_b32_e32 v0, 0x3fff, v0
	v_lshl_add_u32 v0, v0, 9, v118
	global_load_dwordx2 v[70:71], v0, s[82:83]
	v_lshl_add_u32 v0, v1, 9, v118
	global_load_dwordx2 v[72:73], v0, s[82:83]
	v_lshl_add_u32 v0, v2, 9, v118
	global_load_dwordx2 v[74:75], v0, s[82:83]
	v_lshl_add_u32 v0, v3, 9, v118
	global_load_dwordx2 v[80:81], v0, s[82:83]
	ds_read_b128 v[0:3], v135 offset:16
	s_waitcnt vmcnt(8)
	s_and_b32 s2, s5, 0x70000
	s_cmp_eq_u32 s2, 0
	s_cbranch_scc1 .LBB0_2881
	s_bfe_u32 s2, s5, 0x2000e
	s_cmp_eq_u32 s2, 0
	s_cbranch_scc1 .LvB_t0
	s_cmp_eq_u32 s2, 1
	s_cbranch_scc1 .LvB_t1
	s_cmp_eq_u32 s2, 2
	s_cbranch_scc1 .LvB_t2
	s_branch .LvB_t3

; #define LAS __attribute__((address_space(3)))
; #define PE_VMW "vmcnt(" PE_STR(PE_VMY) ")"
; #define PE_WAIT4U(S, cntstr) asm volatile("s_waitcnt " cntstr : "+v"(ru4[S][0]), "+v"(ru4[S][1]), "+v"(ru4[S][2]), "+v"(ru4[S][3]) :: "memory")
;     ...
;         for (int bi = 0; bi < nb; bi += PE_RD) {
; #pragma unroll
;             for (int q = 0; q < PE_RD; ++q) {
;                 PE_WAIT4U(q, PE_VMW);
;                 PE_VBATCH(q, er[q]);
;                 er[q] = __builtin_amdgcn_readfirstlane(nrec.x);
;                 PE_ISSUE4(q, nrec, VB8);
;                 nrec = *(const LAS v4u*)(ents + 4 * (bi + q + PE_RD + 1));
;             }
.LBB0_2881:
	s_waitcnt lgkmcnt(0)
	v_readfirstlane_b32 s5, v0
	v_and_b32_e32 v0, 0x3fff, v0
	v_lshl_add_u32 v0, v0, 9, v118
	global_load_dwordx2 v[76:77], v0, s[82:83]
	v_lshl_add_u32 v0, v1, 9, v118
	global_load_dwordx2 v[82:83], v0, s[82:83]
	v_lshl_add_u32 v0, v2, 9, v118
	global_load_dwordx2 v[84:85], v0, s[82:83]
	v_lshl_add_u32 v0, v3, 9, v118
	global_load_dwordx2 v[90:91], v0, s[82:83]
	ds_read_b128 v[0:3], v135 offset:32
	s_waitcnt vmcnt(8)
	s_and_b32 s2, s8, 0x70000
	s_cmp_eq_u32 s2, 0
	s_cbranch_scc1 .LBB0_2872
	s_bfe_u32 s2, s8, 0x2000e
	s_cmp_eq_u32 s2, 0
	s_cbranch_scc1 .LvC_t0
	s_cmp_eq_u32 s2, 1
	s_cbranch_scc1 .LvC_t1
	s_cmp_eq_u32 s2, 2
	s_cbranch_scc1 .LvC_t2
	s_branch .LvC_t3
